# prologue modulation GEMV: weight loads double-buffered (16 in flight), same accumulation order
# baseline (speedup 1.0000x reference)
; __global__ void __launch_bounds__(512, 2) mega(Args a) {
;     ...
;             for (int it = bx; it < 4 * 96; it += G) {
;                 const int l = it / 96, j0 = (it % 96) * 64;
;                 const float* wp = a.in[I_ADAW] + (size_t)l * 1024 * 6144 + j0 + lane;
;                 float s0 = 0, s1 = 0, s2 = 0, s3 = 0, s4 = 0;
; #pragma unroll 8
;                 for (int kk = 0; kk < 128; ++kk) { const int k = wave * 128 + kk; const float w = wp[(size_t)k * 6144];
;                     s0 += sc[k] * w; s1 += sc[1024 + k] * w; s2 += sc[2048 + k] * w; s3 += sc[3072 + k] * w; s4 += sc[4096 + k] * w; }
.LBB0_19:
	s_mul_hi_i32 s4, s38, 0x2aaaaaab
	s_lshr_b32 s5, s4, 31
	s_ashr_i32 s4, s4, 4
	s_add_i32 s39, s4, s5
	s_mul_i32 s4, s39, 0x60
	s_sub_i32 s4, s38, s4
	s_lshl_b32 s26, s4, 6
	s_ashr_i32 s27, s26, 31
	s_mul_i32 s29, s39, 0x1800000
	s_lshl_b64 s[4:5], s[26:27], 2
	s_mul_hi_i32 s28, s39, 0x1800000
	s_add_u32 s4, s29, s4
	s_addc_u32 s5, s28, s5
	v_mov_b32_e32 v2, 0
	v_lshl_add_u64 v[12:13], v[10:11], 0, s[4:5]
	s_mov_b64 s[28:29], 0
	s_mov_b32 s40, s30
	v_mov_b32_e32 v14, 0
	v_mov_b32_e32 v15, v2
	v_mov_b32_e32 v16, 0
	v_mov_b32_e32 v17, v2
	v_lshl_add_u64 v[18:19], v[12:13], 0, s[28:29]
	s_nop 0
	v_add_co_u32_e64 v20, s[4:5], s15, v18
	global_load_dword v58, v[18:19], off
	s_nop 0
	v_addc_co_u32_e64 v21, s[4:5], 0, v19, s[4:5]
	v_add_co_u32_e64 v22, s[4:5], s31, v18
	s_nop 1
	v_addc_co_u32_e64 v23, s[4:5], 0, v19, s[4:5]
	v_add_co_u32_e64 v24, s[4:5], s33, v18
	s_nop 1
	v_addc_co_u32_e64 v25, s[4:5], 0, v19, s[4:5]
	v_add_co_u32_e64 v26, s[4:5], s34, v18
	s_nop 1
	v_addc_co_u32_e64 v27, s[4:5], 0, v19, s[4:5]
	v_add_co_u32_e64 v28, s[4:5], s35, v18
	s_nop 1
	v_addc_co_u32_e64 v29, s[4:5], 0, v19, s[4:5]
	v_add_co_u32_e64 v30, s[4:5], s36, v18
	s_nop 1
	v_addc_co_u32_e64 v31, s[4:5], 0, v19, s[4:5]
	v_add_co_u32_e64 v18, s[4:5], s37, v18
	s_nop 1
	v_addc_co_u32_e64 v19, s[4:5], 0, v19, s[4:5]
	global_load_dword v60, v[20:21], off
	global_load_dword v62, v[22:23], off
	global_load_dword v64, v[24:25], off
	global_load_dword v66, v[26:27], off
	global_load_dword v68, v[28:29], off
	global_load_dword v70, v[30:31], off
	global_load_dword v72, v[18:19], off
.LBB0_20:
	s_add_u32 s28, s28, 0x30000
	s_addc_u32 s29, s29, 0
	v_mov_b32_e32 v9, s40
	s_add_i32 s40, s40, 32
	v_lshl_add_u64 v[18:19], v[12:13], 0, s[28:29]
	s_nop 0
	v_add_co_u32_e64 v20, s[4:5], s15, v18
	global_load_dword v59, v[18:19], off
	s_nop 0
	v_addc_co_u32_e64 v21, s[4:5], 0, v19, s[4:5]
	v_add_co_u32_e64 v22, s[4:5], s31, v18
	s_nop 1
	v_addc_co_u32_e64 v23, s[4:5], 0, v19, s[4:5]
	v_add_co_u32_e64 v24, s[4:5], s33, v18
	s_nop 1
	v_addc_co_u32_e64 v25, s[4:5], 0, v19, s[4:5]
	v_add_co_u32_e64 v26, s[4:5], s34, v18
	s_nop 1
	v_addc_co_u32_e64 v27, s[4:5], 0, v19, s[4:5]
	v_add_co_u32_e64 v28, s[4:5], s35, v18
	s_nop 1
	v_addc_co_u32_e64 v29, s[4:5], 0, v19, s[4:5]
	v_add_co_u32_e64 v30, s[4:5], s36, v18
	s_nop 1
	v_addc_co_u32_e64 v31, s[4:5], 0, v19, s[4:5]
	v_add_co_u32_e64 v18, s[4:5], s37, v18
	s_nop 1
	v_addc_co_u32_e64 v19, s[4:5], 0, v19, s[4:5]
	global_load_dword v61, v[20:21], off
	global_load_dword v63, v[22:23], off
	global_load_dword v65, v[24:25], off
	global_load_dword v67, v[26:27], off
	global_load_dword v69, v[28:29], off
	global_load_dword v71, v[30:31], off
	global_load_dword v73, v[18:19], off
	ds_read_b128 v[18:21], v9
	ds_read_b128 v[22:25], v9 offset:16
	ds_read_b128 v[26:29], v9 offset:4096
	ds_read_b128 v[30:33], v9 offset:4112
	ds_read_b128 v[34:37], v9 offset:8192
	ds_read_b128 v[38:41], v9 offset:8208
	ds_read_b128 v[42:45], v9 offset:12288
	ds_read_b128 v[46:49], v9 offset:12304
	ds_read_b128 v[50:53], v9 offset:16384
	ds_read_b128 v[54:57], v9 offset:16400
	s_waitcnt lgkmcnt(9)
	v_mov_b32_e32 v74, v18
	s_waitcnt lgkmcnt(7)
	v_mov_b32_e32 v75, v26
	v_mov_b32_e32 v26, v19
	v_mov_b32_e32 v18, v20
	v_mov_b32_e32 v19, v28
	v_mov_b32_e32 v28, v21
	s_waitcnt lgkmcnt(5)
	v_mov_b32_e32 v20, v34
	s_waitcnt lgkmcnt(3)
	v_mov_b32_e32 v21, v42
	v_mov_b32_e32 v42, v35
	v_mov_b32_e32 v34, v36
	v_mov_b32_e32 v35, v44
	v_mov_b32_e32 v44, v37
	v_mov_b32_e32 v36, v22
	v_mov_b32_e32 v37, v30
	v_mov_b32_e32 v30, v23
	v_mov_b32_e32 v22, v24
	v_mov_b32_e32 v23, v32
	v_mov_b32_e32 v32, v25
	v_mov_b32_e32 v24, v38
	s_waitcnt lgkmcnt(2)
	v_mov_b32_e32 v25, v46
	v_mov_b32_e32 v46, v39
	v_mov_b32_e32 v38, v40
	v_mov_b32_e32 v39, v48
	v_mov_b32_e32 v48, v41
	s_waitcnt vmcnt(15)
	v_pk_fma_f32 v[14:15], v[58:59], v[74:75], v[14:15] op_sel_hi:[0,1,1]
	v_pk_fma_f32 v[16:17], v[58:59], v[20:21], v[16:17] op_sel_hi:[0,1,1]
	s_waitcnt lgkmcnt(1)
	v_fmac_f32_e32 v2, v58, v50
	s_waitcnt vmcnt(14)
	v_pk_fma_f32 v[14:15], v[60:61], v[26:27], v[14:15] op_sel_hi:[0,1,1]
	v_pk_fma_f32 v[16:17], v[60:61], v[42:43], v[16:17] op_sel_hi:[0,1,1]
	v_fmac_f32_e32 v2, v60, v51
	s_waitcnt vmcnt(13)
	v_pk_fma_f32 v[14:15], v[62:63], v[18:19], v[14:15] op_sel_hi:[0,1,1]
	v_pk_fma_f32 v[16:17], v[62:63], v[34:35], v[16:17] op_sel_hi:[0,1,1]
	v_fmac_f32_e32 v2, v62, v52
	s_waitcnt vmcnt(12)
	v_pk_fma_f32 v[14:15], v[64:65], v[28:29], v[14:15] op_sel_hi:[0,1,1]
	v_pk_fma_f32 v[16:17], v[64:65], v[44:45], v[16:17] op_sel_hi:[0,1,1]
	v_fmac_f32_e32 v2, v64, v53
	s_waitcnt vmcnt(11)
	v_pk_fma_f32 v[14:15], v[66:67], v[36:37], v[14:15] op_sel_hi:[0,1,1]
	v_pk_fma_f32 v[16:17], v[66:67], v[24:25], v[16:17] op_sel_hi:[0,1,1]
	s_waitcnt lgkmcnt(0)
	v_fmac_f32_e32 v2, v66, v54
	s_waitcnt vmcnt(10)
	v_pk_fma_f32 v[14:15], v[68:69], v[30:31], v[14:15] op_sel_hi:[0,1,1]
	v_pk_fma_f32 v[16:17], v[68:69], v[46:47], v[16:17] op_sel_hi:[0,1,1]
	v_fmac_f32_e32 v2, v68, v55
	s_waitcnt vmcnt(9)
	v_pk_fma_f32 v[14:15], v[70:71], v[22:23], v[14:15] op_sel_hi:[0,1,1]
	v_pk_fma_f32 v[16:17], v[70:71], v[38:39], v[16:17] op_sel_hi:[0,1,1]
	v_fmac_f32_e32 v2, v70, v56
	s_waitcnt vmcnt(8)
; __global__ void __launch_bounds__(512, 2) mega(Args a) {
;     ...
; #pragma unroll 8
;                 for (int kk = 0; kk < 128; ++kk) { const int k = wave * 128 + kk; const float w = wp[(size_t)k * 6144];
;                     s0 += sc[k] * w; s1 += sc[1024 + k] * w; s2 += sc[2048 + k] * w; s3 += sc[3072 + k] * w; s4 += sc[4096 + k] * w; }
;                 red[(wave * 5 + 0) * 64 + lane] = s0; red[(wave * 5 + 1) * 64 + lane] = s1; red[(wave * 5 + 2) * 64 + lane] = s2; red[(wave * 5 + 3) * 64 + lane] = s3; red[(wave * 5 + 4) * 64 + lane] = s4;
;                 __syncthreads();
;                 if (tid < 320) { const int s = tid >> 6, jl = tid & 63; float v = 0;
; #pragma unroll
;                     for (int w = 0; w < 8; ++w) v += red[(w * 5 + s) * 64 + jl];
;                     MOD[((size_t)l * 5 + s) * 6144 + j0 + jl] = v + a.in[I_ADAB][l * 6144 + j0 + jl]; }
	v_pk_fma_f32 v[14:15], v[72:73], v[32:33], v[14:15] op_sel_hi:[0,1,1]
	v_pk_fma_f32 v[16:17], v[72:73], v[48:49], v[16:17] op_sel_hi:[0,1,1]
	v_fmac_f32_e32 v2, v72, v57
	s_add_u32 s28, s28, 0x30000
	s_addc_u32 s29, s29, 0
	s_cmp_eq_u32 s28, 0x300000
	s_cselect_b32 s4, 0, s28
	s_cselect_b32 s5, 0, s29
	v_mov_b32_e32 v9, s40
	s_add_i32 s40, s40, 32
	v_lshl_add_u64 v[18:19], v[12:13], 0, s[4:5]
	s_nop 0
	v_add_co_u32_e64 v20, s[4:5], s15, v18
	global_load_dword v58, v[18:19], off
	s_nop 0
	v_addc_co_u32_e64 v21, s[4:5], 0, v19, s[4:5]
	v_add_co_u32_e64 v22, s[4:5], s31, v18
	s_nop 1
	v_addc_co_u32_e64 v23, s[4:5], 0, v19, s[4:5]
	v_add_co_u32_e64 v24, s[4:5], s33, v18
	s_nop 1
	v_addc_co_u32_e64 v25, s[4:5], 0, v19, s[4:5]
	v_add_co_u32_e64 v26, s[4:5], s34, v18
	s_nop 1
	v_addc_co_u32_e64 v27, s[4:5], 0, v19, s[4:5]
	v_add_co_u32_e64 v28, s[4:5], s35, v18
	s_nop 1
	v_addc_co_u32_e64 v29, s[4:5], 0, v19, s[4:5]
	v_add_co_u32_e64 v30, s[4:5], s36, v18
	s_nop 1
	v_addc_co_u32_e64 v31, s[4:5], 0, v19, s[4:5]
	v_add_co_u32_e64 v18, s[4:5], s37, v18
	s_nop 1
	v_addc_co_u32_e64 v19, s[4:5], 0, v19, s[4:5]
	global_load_dword v60, v[20:21], off
	global_load_dword v62, v[22:23], off
	global_load_dword v64, v[24:25], off
	global_load_dword v66, v[26:27], off
	global_load_dword v68, v[28:29], off
	global_load_dword v70, v[30:31], off
	global_load_dword v72, v[18:19], off
	ds_read_b128 v[18:21], v9
	ds_read_b128 v[22:25], v9 offset:16
	ds_read_b128 v[26:29], v9 offset:4096
	ds_read_b128 v[30:33], v9 offset:4112
	ds_read_b128 v[34:37], v9 offset:8192
	ds_read_b128 v[38:41], v9 offset:8208
	ds_read_b128 v[42:45], v9 offset:12288
	ds_read_b128 v[46:49], v9 offset:12304
	ds_read_b128 v[50:53], v9 offset:16384
	ds_read_b128 v[54:57], v9 offset:16400
	s_waitcnt lgkmcnt(9)
	v_mov_b32_e32 v74, v18
	s_waitcnt lgkmcnt(7)
	v_mov_b32_e32 v75, v26
	v_mov_b32_e32 v26, v19
	v_mov_b32_e32 v18, v20
	v_mov_b32_e32 v19, v28
	v_mov_b32_e32 v28, v21
	s_waitcnt lgkmcnt(5)
	v_mov_b32_e32 v20, v34
	s_waitcnt lgkmcnt(3)
	v_mov_b32_e32 v21, v42
	v_mov_b32_e32 v42, v35
	v_mov_b32_e32 v34, v36
	v_mov_b32_e32 v35, v44
	v_mov_b32_e32 v44, v37
	v_mov_b32_e32 v36, v22
	v_mov_b32_e32 v37, v30
	v_mov_b32_e32 v30, v23
	v_mov_b32_e32 v22, v24
	v_mov_b32_e32 v23, v32
	v_mov_b32_e32 v32, v25
	v_mov_b32_e32 v24, v38
	s_waitcnt lgkmcnt(2)
	v_mov_b32_e32 v25, v46
	v_mov_b32_e32 v46, v39
	v_mov_b32_e32 v38, v40
	v_mov_b32_e32 v39, v48
	v_mov_b32_e32 v48, v41
	s_waitcnt vmcnt(15)
	v_pk_fma_f32 v[14:15], v[58:59], v[74:75], v[14:15] op_sel:[1,0,0] op_sel_hi:[1,1,1]
	v_pk_fma_f32 v[16:17], v[58:59], v[20:21], v[16:17] op_sel:[1,0,0] op_sel_hi:[1,1,1]
	s_waitcnt lgkmcnt(1)
	v_fmac_f32_e32 v2, v59, v50
	s_waitcnt vmcnt(14)
	v_pk_fma_f32 v[14:15], v[60:61], v[26:27], v[14:15] op_sel:[1,0,0] op_sel_hi:[1,1,1]
	v_pk_fma_f32 v[16:17], v[60:61], v[42:43], v[16:17] op_sel:[1,0,0] op_sel_hi:[1,1,1]
	v_fmac_f32_e32 v2, v61, v51
	s_waitcnt vmcnt(13)
	v_pk_fma_f32 v[14:15], v[62:63], v[18:19], v[14:15] op_sel:[1,0,0] op_sel_hi:[1,1,1]
	v_pk_fma_f32 v[16:17], v[62:63], v[34:35], v[16:17] op_sel:[1,0,0] op_sel_hi:[1,1,1]
	v_fmac_f32_e32 v2, v63, v52
	s_waitcnt vmcnt(12)
	v_pk_fma_f32 v[14:15], v[64:65], v[28:29], v[14:15] op_sel:[1,0,0] op_sel_hi:[1,1,1]
	v_pk_fma_f32 v[16:17], v[64:65], v[44:45], v[16:17] op_sel:[1,0,0] op_sel_hi:[1,1,1]
	v_fmac_f32_e32 v2, v65, v53
	s_waitcnt vmcnt(11)
	v_pk_fma_f32 v[14:15], v[66:67], v[36:37], v[14:15] op_sel:[1,0,0] op_sel_hi:[1,1,1]
	v_pk_fma_f32 v[16:17], v[66:67], v[24:25], v[16:17] op_sel:[1,0,0] op_sel_hi:[1,1,1]
	s_waitcnt lgkmcnt(0)
	v_fmac_f32_e32 v2, v67, v54
	s_waitcnt vmcnt(10)
	v_pk_fma_f32 v[14:15], v[68:69], v[30:31], v[14:15] op_sel:[1,0,0] op_sel_hi:[1,1,1]
	v_pk_fma_f32 v[16:17], v[68:69], v[46:47], v[16:17] op_sel:[1,0,0] op_sel_hi:[1,1,1]
	v_fmac_f32_e32 v2, v69, v55
	s_waitcnt vmcnt(9)
	v_pk_fma_f32 v[14:15], v[70:71], v[22:23], v[14:15] op_sel:[1,0,0] op_sel_hi:[1,1,1]
	v_pk_fma_f32 v[16:17], v[70:71], v[38:39], v[16:17] op_sel:[1,0,0] op_sel_hi:[1,1,1]
	v_fmac_f32_e32 v2, v71, v56
	s_waitcnt vmcnt(8)
	v_pk_fma_f32 v[14:15], v[72:73], v[32:33], v[14:15] op_sel:[1,0,0] op_sel_hi:[1,1,1]
	v_pk_fma_f32 v[16:17], v[72:73], v[48:49], v[16:17] op_sel:[1,0,0] op_sel_hi:[1,1,1]
	v_fmac_f32_e32 v2, v73, v57
	s_cmp_eq_u32 s28, 0x300000
	s_cbranch_scc0 .LBB0_20
	s_waitcnt vmcnt(0)
	ds_write2st64_b32 v1, v14, v15 offset0:80 offset1:81
	ds_write2st64_b32 v1, v16, v17 offset0:82 offset1:83
	ds_write_b32 v1, v2 offset:21504
	s_waitcnt lgkmcnt(0)
	s_barrier
	s_and_saveexec_b64 s[4:5], vcc
	s_cbranch_execz .LBB0_18
	s_mul_i32 s28, s39, 0x1800
	s_add_i32 s28, s28, s26
	v_or_b32_e32 v12, s28, v8
	v_ashrrev_i32_e32 v13, 31, v12
	v_lshl_add_u64 v[12:13], v[12:13], 2, s[6:7]
	global_load_dword v9, v[12:13], off
	ds_read2st64_b32 v[12:13], v5 offset0:80 offset1:85
	ds_read2st64_b32 v[14:15], v5 offset0:90 offset1:95
	ds_read2st64_b32 v[16:17], v5 offset0:100 offset1:105
	ds_read2st64_b32 v[18:19], v5 offset0:110 offset1:115
	v_mad_i64_i32 v[20:21], s[28:29], s39, 5, v[6:7]
	s_waitcnt lgkmcnt(3)
	v_add_f32_e32 v12, 0, v12
	v_add_f32_e32 v12, v12, v13
	s_waitcnt lgkmcnt(2)
	v_add_f32_e32 v12, v12, v14
	v_add_f32_e32 v12, v12, v15
	v_mov_b64_e32 v[22:23], s[72:73]
	s_waitcnt lgkmcnt(1)
	v_add_f32_e32 v12, v12, v16
	v_mad_u64_u32 v[22:23], s[28:29], v20, s15, v[22:23]
	v_add_f32_e32 v12, v12, v17
	v_mad_i32_i24 v23, v21, s15, v23
	s_waitcnt lgkmcnt(0)
	v_add_f32_e32 v12, v12, v18
	v_lshlrev_b32_e32 v2, 2, v8
	v_lshl_add_u64 v[20:21], s[26:27], 2, v[22:23]
	v_add_f32_e32 v12, v12, v19
	s_waitcnt vmcnt(0)
	v_add_f32_e32 v9, v12, v9
	v_lshl_add_u64 v[12:13], v[20:21], 0, v[2:3]
	global_store_dword v[12:13], v9, off
	s_branch .LBB0_18
